# gate_up epilogue rewritten by hand: scalar f32, 4 elements interleaved; 1.702*log2e folded into one constant; up+1 folded into bias (clamp -6..8)
# speedup vs baseline: 1.0284x; 1.0063x over previous
.LBB0_1246:
	s_mov_b32 s21, -1
	s_mov_b64 s[28:29], s[96:97]
	s_load_dwordx2 s[30:31], s[28:29], 0xc0
	v_mbcnt_lo_u32_b32 v0, s21, 0
	v_mbcnt_hi_u32_b32 v0, s21, v0
	v_lshrrev_b32_e32 v67, 1, v0
	v_and_or_b32 v0, v0, 15, s50
	s_waitcnt lgkmcnt(0)
	s_add_u32 s30, s30, s18
	s_addc_u32 s31, s31, s19
	s_lshl_b32 s21, s26, 7
	v_and_or_b32 v67, v67, 24, s21
	v_or_b32_e32 v146, s51, v67
	v_ashrrev_i32_e32 v67, 31, v66
	v_lshlrev_b64 v[66:67], 13, v[66:67]
	v_lshlrev_b32_e32 v68, 1, v146
	v_lshl_add_u64 v[66:67], s[30:31], 0, v[66:67]
	v_ashrrev_i32_e32 v69, 31, v68
	v_lshl_add_u64 v[66:67], v[68:69], 2, v[66:67]
	global_load_dwordx4 v[90:93], v[66:67], off
	global_load_dwordx4 v[82:85], v[66:67], off offset:16
	global_load_dwordx4 v[74:77], v[66:67], off offset:32
	s_nop 0
	global_load_dwordx4 v[66:69], v[66:67], off offset:48
	s_load_dwordx2 s[28:29], s[28:29], 0xe8
	v_ashrrev_i32_e32 v147, 31, v146
	s_andn2_b64 vcc, exec, s[2:3]
	s_mov_b64 s[2:3], -1
	s_mov_b64 s[68:69], s[94:95]
	s_waitcnt lgkmcnt(0)
	v_lshl_add_u64 v[146:147], s[28:29], 0, v[146:147]
	s_mov_b64 s[28:29], 0x72b00000
	v_lshl_add_u64 v[146:147], v[146:147], 0, s[28:29]
	v_mov_b32_e32 v240, v243
	s_waitcnt vmcnt(0)
	s_mov_b32 s99, 0
	s_mov_b32 s72, 0xc0c00000
	v_mov_b32_e32 v178, 0x41000000
	v_add_f32_e32 v91, 1.0, v91
	v_add_f32_e32 v93, 1.0, v93
	v_add_f32_e32 v83, 1.0, v83
	v_add_f32_e32 v85, 1.0, v85
	v_add_f32_e32 v75, 1.0, v75
	v_add_f32_e32 v77, 1.0, v77
	v_add_f32_e32 v67, 1.0, v67
	v_add_f32_e32 v69, 1.0, v69
	v_lshl_add_u32 v176, s62, 8, v0
	v_ashrrev_i32_e32 v177, 31, v176
	v_lshlrev_b64 v[176:177], 10, v[176:177]
	v_lshl_add_u64 v[176:177], v[146:147], 0, v[176:177]
	s_mov_b32 s98, 0x0
	v_lshl_add_u64 v[192:193], v[176:177], 0, s[98:99]
	v_fmamk_f32 v142, v142, 0x3d000000, v90
	v_fmamk_f32 v143, v143, 0x3d000000, v92
	v_fmamk_f32 v144, v144, 0x3d000000, v82
	v_fmamk_f32 v145, v145, 0x3d000000, v84
	v_min_f32_e32 v142, 0x40e00000, v142
	v_min_f32_e32 v143, 0x40e00000, v143
	v_min_f32_e32 v144, 0x40e00000, v144
	v_min_f32_e32 v145, 0x40e00000, v145
	v_mul_f32_e32 v180, 0xc01d265f, v142
	v_mul_f32_e32 v181, 0xc01d265f, v143
	v_mul_f32_e32 v182, 0xc01d265f, v144
	v_mul_f32_e32 v183, 0xc01d265f, v145
	v_exp_f32_e32 v180, v180
	v_exp_f32_e32 v181, v181
	v_exp_f32_e32 v182, v182
	v_exp_f32_e32 v183, v183
	v_fmamk_f32 v138, v138, 0x3d000000, v91
	v_fmamk_f32 v139, v139, 0x3d000000, v93
	v_fmamk_f32 v140, v140, 0x3d000000, v83
	v_fmamk_f32 v141, v141, 0x3d000000, v85
	v_add_f32_e32 v180, 1.0, v180
	v_add_f32_e32 v181, 1.0, v181
	v_add_f32_e32 v182, 1.0, v182
	v_add_f32_e32 v183, 1.0, v183
	v_rcp_f32_e32 v180, v180
	v_rcp_f32_e32 v181, v181
	v_rcp_f32_e32 v182, v182
	v_rcp_f32_e32 v183, v183
	v_med3_f32 v138, v138, s72, v178
	v_med3_f32 v139, v139, s72, v178
	v_med3_f32 v140, v140, s72, v178
	v_med3_f32 v141, v141, s72, v178
	v_mul_f32_e32 v180, v142, v180
	v_mul_f32_e32 v181, v143, v181
	v_mul_f32_e32 v182, v144, v182
	v_mul_f32_e32 v183, v145, v183
	v_mul_f32_e32 v180, v138, v180
	v_mul_f32_e32 v181, v139, v181
	v_mul_f32_e32 v182, v140, v182
	v_mul_f32_e32 v183, v141, v183
	v_cvt_pk_fp8_f32 v188, v180, v181
	v_cvt_pk_fp8_f32 v188, v182, v183 op_sel:[0,0,1]
	v_fmamk_f32 v134, v134, 0x3d000000, v74
	v_fmamk_f32 v135, v135, 0x3d000000, v76
	v_fmamk_f32 v136, v136, 0x3d000000, v66
	v_fmamk_f32 v137, v137, 0x3d000000, v68
	v_min_f32_e32 v134, 0x40e00000, v134
	v_min_f32_e32 v135, 0x40e00000, v135
	v_min_f32_e32 v136, 0x40e00000, v136
	v_min_f32_e32 v137, 0x40e00000, v137
	v_mul_f32_e32 v184, 0xc01d265f, v134
	v_mul_f32_e32 v185, 0xc01d265f, v135
	v_mul_f32_e32 v186, 0xc01d265f, v136
	v_mul_f32_e32 v187, 0xc01d265f, v137
	v_exp_f32_e32 v184, v184
	v_exp_f32_e32 v185, v185
	v_exp_f32_e32 v186, v186
	v_exp_f32_e32 v187, v187
	v_fmamk_f32 v130, v130, 0x3d000000, v75
	v_fmamk_f32 v131, v131, 0x3d000000, v77
	v_fmamk_f32 v132, v132, 0x3d000000, v67
	v_fmamk_f32 v133, v133, 0x3d000000, v69
	v_add_f32_e32 v184, 1.0, v184
	v_add_f32_e32 v185, 1.0, v185
	v_add_f32_e32 v186, 1.0, v186
	v_add_f32_e32 v187, 1.0, v187
	v_rcp_f32_e32 v184, v184
	v_rcp_f32_e32 v185, v185
	v_rcp_f32_e32 v186, v186
	v_rcp_f32_e32 v187, v187
	v_med3_f32 v130, v130, s72, v178
	v_med3_f32 v131, v131, s72, v178
	v_med3_f32 v132, v132, s72, v178
	v_med3_f32 v133, v133, s72, v178
	v_mul_f32_e32 v184, v134, v184
	v_mul_f32_e32 v185, v135, v185
	v_mul_f32_e32 v186, v136, v186
	v_mul_f32_e32 v187, v137, v187
	v_mul_f32_e32 v184, v130, v184
	v_mul_f32_e32 v185, v131, v185
	v_mul_f32_e32 v186, v132, v186
	v_mul_f32_e32 v187, v133, v187
	v_cvt_pk_fp8_f32 v189, v184, v185
	v_cvt_pk_fp8_f32 v189, v186, v187 op_sel:[0,0,1]
	global_store_dwordx2 v[192:193], v[188:189], off
	s_mov_b32 s98, 0x4000
	v_lshl_add_u64 v[194:195], v[176:177], 0, s[98:99]
	v_fmamk_f32 v126, v126, 0x3d000000, v90
	v_fmamk_f32 v127, v127, 0x3d000000, v92
	v_fmamk_f32 v128, v128, 0x3d000000, v82
	v_fmamk_f32 v129, v129, 0x3d000000, v84
	v_min_f32_e32 v126, 0x40e00000, v126
	v_min_f32_e32 v127, 0x40e00000, v127
	v_min_f32_e32 v128, 0x40e00000, v128
	v_min_f32_e32 v129, 0x40e00000, v129
	v_mul_f32_e32 v180, 0xc01d265f, v126
	v_mul_f32_e32 v181, 0xc01d265f, v127
	v_mul_f32_e32 v182, 0xc01d265f, v128
	v_mul_f32_e32 v183, 0xc01d265f, v129
	v_exp_f32_e32 v180, v180
	v_exp_f32_e32 v181, v181
	v_exp_f32_e32 v182, v182
	v_exp_f32_e32 v183, v183
	v_fmamk_f32 v122, v122, 0x3d000000, v91
	v_fmamk_f32 v123, v123, 0x3d000000, v93
	v_fmamk_f32 v124, v124, 0x3d000000, v83
	v_fmamk_f32 v125, v125, 0x3d000000, v85
	v_add_f32_e32 v180, 1.0, v180
	v_add_f32_e32 v181, 1.0, v181
	v_add_f32_e32 v182, 1.0, v182
	v_add_f32_e32 v183, 1.0, v183
	v_rcp_f32_e32 v180, v180
	v_rcp_f32_e32 v181, v181
	v_rcp_f32_e32 v182, v182
	v_rcp_f32_e32 v183, v183
	v_med3_f32 v122, v122, s72, v178
	v_med3_f32 v123, v123, s72, v178
	v_med3_f32 v124, v124, s72, v178
	v_med3_f32 v125, v125, s72, v178
	v_mul_f32_e32 v180, v126, v180
	v_mul_f32_e32 v181, v127, v181
	v_mul_f32_e32 v182, v128, v182
	v_mul_f32_e32 v183, v129, v183
	v_mul_f32_e32 v180, v122, v180
	v_mul_f32_e32 v181, v123, v181
	v_mul_f32_e32 v182, v124, v182
	v_mul_f32_e32 v183, v125, v183
	v_cvt_pk_fp8_f32 v190, v180, v181
	v_cvt_pk_fp8_f32 v190, v182, v183 op_sel:[0,0,1]
	v_fmamk_f32 v118, v118, 0x3d000000, v74
	v_fmamk_f32 v119, v119, 0x3d000000, v76
	v_fmamk_f32 v120, v120, 0x3d000000, v66
	v_fmamk_f32 v121, v121, 0x3d000000, v68
	v_min_f32_e32 v118, 0x40e00000, v118
	v_min_f32_e32 v119, 0x40e00000, v119
	v_min_f32_e32 v120, 0x40e00000, v120
	v_min_f32_e32 v121, 0x40e00000, v121
	v_mul_f32_e32 v184, 0xc01d265f, v118
	v_mul_f32_e32 v185, 0xc01d265f, v119
	v_mul_f32_e32 v186, 0xc01d265f, v120
	v_mul_f32_e32 v187, 0xc01d265f, v121
	v_exp_f32_e32 v184, v184
	v_exp_f32_e32 v185, v185
	v_exp_f32_e32 v186, v186
	v_exp_f32_e32 v187, v187
	v_fmamk_f32 v114, v114, 0x3d000000, v75
	v_fmamk_f32 v115, v115, 0x3d000000, v77
	v_fmamk_f32 v116, v116, 0x3d000000, v67
	v_fmamk_f32 v117, v117, 0x3d000000, v69
	v_add_f32_e32 v184, 1.0, v184
	v_add_f32_e32 v185, 1.0, v185
	v_add_f32_e32 v186, 1.0, v186
	v_add_f32_e32 v187, 1.0, v187
	v_rcp_f32_e32 v184, v184
	v_rcp_f32_e32 v185, v185
	v_rcp_f32_e32 v186, v186
	v_rcp_f32_e32 v187, v187
	v_med3_f32 v114, v114, s72, v178
	v_med3_f32 v115, v115, s72, v178
	v_med3_f32 v116, v116, s72, v178
	v_med3_f32 v117, v117, s72, v178
	v_mul_f32_e32 v184, v118, v184
	v_mul_f32_e32 v185, v119, v185
	v_mul_f32_e32 v186, v120, v186
	v_mul_f32_e32 v187, v121, v187
	v_mul_f32_e32 v184, v114, v184
	v_mul_f32_e32 v185, v115, v185
	v_mul_f32_e32 v186, v116, v186
	v_mul_f32_e32 v187, v117, v187
	v_cvt_pk_fp8_f32 v191, v184, v185
	v_cvt_pk_fp8_f32 v191, v186, v187 op_sel:[0,0,1]
	global_store_dwordx2 v[194:195], v[190:191], off
	s_mov_b32 s98, 0x8000
	v_lshl_add_u64 v[196:197], v[176:177], 0, s[98:99]
	v_fmamk_f32 v110, v110, 0x3d000000, v90
	v_fmamk_f32 v111, v111, 0x3d000000, v92
	v_fmamk_f32 v112, v112, 0x3d000000, v82
	v_fmamk_f32 v113, v113, 0x3d000000, v84
	v_min_f32_e32 v110, 0x40e00000, v110
	v_min_f32_e32 v111, 0x40e00000, v111
	v_min_f32_e32 v112, 0x40e00000, v112
	v_min_f32_e32 v113, 0x40e00000, v113
	v_mul_f32_e32 v180, 0xc01d265f, v110
	v_mul_f32_e32 v181, 0xc01d265f, v111
	v_mul_f32_e32 v182, 0xc01d265f, v112
	v_mul_f32_e32 v183, 0xc01d265f, v113
	v_exp_f32_e32 v180, v180
	v_exp_f32_e32 v181, v181
	v_exp_f32_e32 v182, v182
	v_exp_f32_e32 v183, v183
	v_fmamk_f32 v106, v106, 0x3d000000, v91
	v_fmamk_f32 v107, v107, 0x3d000000, v93
	v_fmamk_f32 v108, v108, 0x3d000000, v83
	v_fmamk_f32 v109, v109, 0x3d000000, v85
	v_add_f32_e32 v180, 1.0, v180
	v_add_f32_e32 v181, 1.0, v181
	v_add_f32_e32 v182, 1.0, v182
	v_add_f32_e32 v183, 1.0, v183
	v_rcp_f32_e32 v180, v180
	v_rcp_f32_e32 v181, v181
	v_rcp_f32_e32 v182, v182
	v_rcp_f32_e32 v183, v183
	v_med3_f32 v106, v106, s72, v178
	v_med3_f32 v107, v107, s72, v178
	v_med3_f32 v108, v108, s72, v178
	v_med3_f32 v109, v109, s72, v178
	v_mul_f32_e32 v180, v110, v180
	v_mul_f32_e32 v181, v111, v181
	v_mul_f32_e32 v182, v112, v182
	v_mul_f32_e32 v183, v113, v183
	v_mul_f32_e32 v180, v106, v180
	v_mul_f32_e32 v181, v107, v181
	v_mul_f32_e32 v182, v108, v182
	v_mul_f32_e32 v183, v109, v183
	v_cvt_pk_fp8_f32 v188, v180, v181
	v_cvt_pk_fp8_f32 v188, v182, v183 op_sel:[0,0,1]
	v_fmamk_f32 v102, v102, 0x3d000000, v74
	v_fmamk_f32 v103, v103, 0x3d000000, v76
	v_fmamk_f32 v104, v104, 0x3d000000, v66
	v_fmamk_f32 v105, v105, 0x3d000000, v68
	v_min_f32_e32 v102, 0x40e00000, v102
	v_min_f32_e32 v103, 0x40e00000, v103
	v_min_f32_e32 v104, 0x40e00000, v104
	v_min_f32_e32 v105, 0x40e00000, v105
	v_mul_f32_e32 v184, 0xc01d265f, v102
	v_mul_f32_e32 v185, 0xc01d265f, v103
	v_mul_f32_e32 v186, 0xc01d265f, v104
	v_mul_f32_e32 v187, 0xc01d265f, v105
	v_exp_f32_e32 v184, v184
	v_exp_f32_e32 v185, v185
	v_exp_f32_e32 v186, v186
	v_exp_f32_e32 v187, v187
	v_fmamk_f32 v98, v98, 0x3d000000, v75
	v_fmamk_f32 v99, v99, 0x3d000000, v77
	v_fmamk_f32 v100, v100, 0x3d000000, v67
	v_fmamk_f32 v101, v101, 0x3d000000, v69
	v_add_f32_e32 v184, 1.0, v184
	v_add_f32_e32 v185, 1.0, v185
	v_add_f32_e32 v186, 1.0, v186
	v_add_f32_e32 v187, 1.0, v187
	v_rcp_f32_e32 v184, v184
	v_rcp_f32_e32 v185, v185
	v_rcp_f32_e32 v186, v186
	v_rcp_f32_e32 v187, v187
	v_med3_f32 v98, v98, s72, v178
	v_med3_f32 v99, v99, s72, v178
	v_med3_f32 v100, v100, s72, v178
	v_med3_f32 v101, v101, s72, v178
	v_mul_f32_e32 v184, v102, v184
	v_mul_f32_e32 v185, v103, v185
	v_mul_f32_e32 v186, v104, v186
	v_mul_f32_e32 v187, v105, v187
	v_mul_f32_e32 v184, v98, v184
	v_mul_f32_e32 v185, v99, v185
	v_mul_f32_e32 v186, v100, v186
	v_mul_f32_e32 v187, v101, v187
	v_cvt_pk_fp8_f32 v189, v184, v185
	v_cvt_pk_fp8_f32 v189, v186, v187 op_sel:[0,0,1]
	global_store_dwordx2 v[196:197], v[188:189], off
	s_mov_b32 s98, 0xc000
	v_lshl_add_u64 v[198:199], v[176:177], 0, s[98:99]
	v_fmamk_f32 v94, v94, 0x3d000000, v90
	v_fmamk_f32 v95, v95, 0x3d000000, v92
	v_fmamk_f32 v96, v96, 0x3d000000, v82
	v_fmamk_f32 v97, v97, 0x3d000000, v84
	v_min_f32_e32 v94, 0x40e00000, v94
	v_min_f32_e32 v95, 0x40e00000, v95
	v_min_f32_e32 v96, 0x40e00000, v96
	v_min_f32_e32 v97, 0x40e00000, v97
	v_mul_f32_e32 v180, 0xc01d265f, v94
	v_mul_f32_e32 v181, 0xc01d265f, v95
	v_mul_f32_e32 v182, 0xc01d265f, v96
	v_mul_f32_e32 v183, 0xc01d265f, v97
	v_exp_f32_e32 v180, v180
	v_exp_f32_e32 v181, v181
	v_exp_f32_e32 v182, v182
	v_exp_f32_e32 v183, v183
	v_fmamk_f32 v86, v86, 0x3d000000, v91
	v_fmamk_f32 v87, v87, 0x3d000000, v93
	v_fmamk_f32 v88, v88, 0x3d000000, v83
	v_fmamk_f32 v89, v89, 0x3d000000, v85
	v_add_f32_e32 v180, 1.0, v180
	v_add_f32_e32 v181, 1.0, v181
	v_add_f32_e32 v182, 1.0, v182
	v_add_f32_e32 v183, 1.0, v183
	v_rcp_f32_e32 v180, v180
	v_rcp_f32_e32 v181, v181
	v_rcp_f32_e32 v182, v182
	v_rcp_f32_e32 v183, v183
	v_med3_f32 v86, v86, s72, v178
	v_med3_f32 v87, v87, s72, v178
	v_med3_f32 v88, v88, s72, v178
	v_med3_f32 v89, v89, s72, v178
	v_mul_f32_e32 v180, v94, v180
	v_mul_f32_e32 v181, v95, v181
	v_mul_f32_e32 v182, v96, v182
	v_mul_f32_e32 v183, v97, v183
	v_mul_f32_e32 v180, v86, v180
	v_mul_f32_e32 v181, v87, v181
	v_mul_f32_e32 v182, v88, v182
	v_mul_f32_e32 v183, v89, v183
	v_cvt_pk_fp8_f32 v190, v180, v181
	v_cvt_pk_fp8_f32 v190, v182, v183 op_sel:[0,0,1]
	v_fmamk_f32 v78, v78, 0x3d000000, v74
	v_fmamk_f32 v79, v79, 0x3d000000, v76
	v_fmamk_f32 v80, v80, 0x3d000000, v66
	v_fmamk_f32 v81, v81, 0x3d000000, v68
	v_min_f32_e32 v78, 0x40e00000, v78
	v_min_f32_e32 v79, 0x40e00000, v79
	v_min_f32_e32 v80, 0x40e00000, v80
	v_min_f32_e32 v81, 0x40e00000, v81
	v_mul_f32_e32 v184, 0xc01d265f, v78
	v_mul_f32_e32 v185, 0xc01d265f, v79
	v_mul_f32_e32 v186, 0xc01d265f, v80
	v_mul_f32_e32 v187, 0xc01d265f, v81
	v_exp_f32_e32 v184, v184
	v_exp_f32_e32 v185, v185
	v_exp_f32_e32 v186, v186
	v_exp_f32_e32 v187, v187
	v_fmamk_f32 v70, v70, 0x3d000000, v75
	v_fmamk_f32 v71, v71, 0x3d000000, v77
	v_fmamk_f32 v72, v72, 0x3d000000, v67
	v_fmamk_f32 v73, v73, 0x3d000000, v69
	v_add_f32_e32 v184, 1.0, v184
	v_add_f32_e32 v185, 1.0, v185
	v_add_f32_e32 v186, 1.0, v186
	v_add_f32_e32 v187, 1.0, v187
	v_rcp_f32_e32 v184, v184
	v_rcp_f32_e32 v185, v185
	v_rcp_f32_e32 v186, v186
	v_rcp_f32_e32 v187, v187
	v_med3_f32 v70, v70, s72, v178
	v_med3_f32 v71, v71, s72, v178
	v_med3_f32 v72, v72, s72, v178
	v_med3_f32 v73, v73, s72, v178
	v_mul_f32_e32 v184, v78, v184
	v_mul_f32_e32 v185, v79, v185
	v_mul_f32_e32 v186, v80, v186
	v_mul_f32_e32 v187, v81, v187
	v_mul_f32_e32 v184, v70, v184
	v_mul_f32_e32 v185, v71, v185
	v_mul_f32_e32 v186, v72, v186
	v_mul_f32_e32 v187, v73, v187
	v_cvt_pk_fp8_f32 v191, v184, v185
	v_cvt_pk_fp8_f32 v191, v186, v187 op_sel:[0,0,1]
	global_store_dwordx2 v[198:199], v[190:191], off
	s_mov_b32 s98, 0x20000
	v_lshl_add_u64 v[192:193], v[176:177], 0, s[98:99]
	v_fmamk_f32 v62, v62, 0x3d000000, v90
	v_fmamk_f32 v63, v63, 0x3d000000, v92
	v_fmamk_f32 v64, v64, 0x3d000000, v82
	v_fmamk_f32 v65, v65, 0x3d000000, v84
	v_min_f32_e32 v62, 0x40e00000, v62
	v_min_f32_e32 v63, 0x40e00000, v63
	v_min_f32_e32 v64, 0x40e00000, v64
	v_min_f32_e32 v65, 0x40e00000, v65
	v_mul_f32_e32 v180, 0xc01d265f, v62
	v_mul_f32_e32 v181, 0xc01d265f, v63
	v_mul_f32_e32 v182, 0xc01d265f, v64
	v_mul_f32_e32 v183, 0xc01d265f, v65
	v_exp_f32_e32 v180, v180
	v_exp_f32_e32 v181, v181
	v_exp_f32_e32 v182, v182
	v_exp_f32_e32 v183, v183
	v_fmamk_f32 v58, v58, 0x3d000000, v91
	v_fmamk_f32 v59, v59, 0x3d000000, v93
	v_fmamk_f32 v60, v60, 0x3d000000, v83
	v_fmamk_f32 v61, v61, 0x3d000000, v85
	v_add_f32_e32 v180, 1.0, v180
	v_add_f32_e32 v181, 1.0, v181
	v_add_f32_e32 v182, 1.0, v182
	v_add_f32_e32 v183, 1.0, v183
	v_rcp_f32_e32 v180, v180
	v_rcp_f32_e32 v181, v181
	v_rcp_f32_e32 v182, v182
	v_rcp_f32_e32 v183, v183
	v_med3_f32 v58, v58, s72, v178
	v_med3_f32 v59, v59, s72, v178
	v_med3_f32 v60, v60, s72, v178
	v_med3_f32 v61, v61, s72, v178
	v_mul_f32_e32 v180, v62, v180
	v_mul_f32_e32 v181, v63, v181
	v_mul_f32_e32 v182, v64, v182
	v_mul_f32_e32 v183, v65, v183
	v_mul_f32_e32 v180, v58, v180
	v_mul_f32_e32 v181, v59, v181
	v_mul_f32_e32 v182, v60, v182
	v_mul_f32_e32 v183, v61, v183
	v_cvt_pk_fp8_f32 v188, v180, v181
	v_cvt_pk_fp8_f32 v188, v182, v183 op_sel:[0,0,1]
	v_fmamk_f32 v54, v54, 0x3d000000, v74
	v_fmamk_f32 v55, v55, 0x3d000000, v76
	v_fmamk_f32 v56, v56, 0x3d000000, v66
	v_fmamk_f32 v57, v57, 0x3d000000, v68
	v_min_f32_e32 v54, 0x40e00000, v54
	v_min_f32_e32 v55, 0x40e00000, v55
	v_min_f32_e32 v56, 0x40e00000, v56
	v_min_f32_e32 v57, 0x40e00000, v57
	v_mul_f32_e32 v184, 0xc01d265f, v54
	v_mul_f32_e32 v185, 0xc01d265f, v55
	v_mul_f32_e32 v186, 0xc01d265f, v56
	v_mul_f32_e32 v187, 0xc01d265f, v57
	v_exp_f32_e32 v184, v184
	v_exp_f32_e32 v185, v185
	v_exp_f32_e32 v186, v186
	v_exp_f32_e32 v187, v187
	v_fmamk_f32 v50, v50, 0x3d000000, v75
	v_fmamk_f32 v51, v51, 0x3d000000, v77
	v_fmamk_f32 v52, v52, 0x3d000000, v67
	v_fmamk_f32 v53, v53, 0x3d000000, v69
	v_add_f32_e32 v184, 1.0, v184
	v_add_f32_e32 v185, 1.0, v185
	v_add_f32_e32 v186, 1.0, v186
	v_add_f32_e32 v187, 1.0, v187
	v_rcp_f32_e32 v184, v184
	v_rcp_f32_e32 v185, v185
	v_rcp_f32_e32 v186, v186
	v_rcp_f32_e32 v187, v187
	v_med3_f32 v50, v50, s72, v178
	v_med3_f32 v51, v51, s72, v178
	v_med3_f32 v52, v52, s72, v178
	v_med3_f32 v53, v53, s72, v178
	v_mul_f32_e32 v184, v54, v184
	v_mul_f32_e32 v185, v55, v185
	v_mul_f32_e32 v186, v56, v186
	v_mul_f32_e32 v187, v57, v187
	v_mul_f32_e32 v184, v50, v184
	v_mul_f32_e32 v185, v51, v185
	v_mul_f32_e32 v186, v52, v186
	v_mul_f32_e32 v187, v53, v187
	v_cvt_pk_fp8_f32 v189, v184, v185
	v_cvt_pk_fp8_f32 v189, v186, v187 op_sel:[0,0,1]
	global_store_dwordx2 v[192:193], v[188:189], off
	s_mov_b32 s98, 0x24000
	v_lshl_add_u64 v[194:195], v[176:177], 0, s[98:99]
	v_fmamk_f32 v46, v46, 0x3d000000, v90
	v_fmamk_f32 v47, v47, 0x3d000000, v92
	v_fmamk_f32 v48, v48, 0x3d000000, v82
	v_fmamk_f32 v49, v49, 0x3d000000, v84
	v_min_f32_e32 v46, 0x40e00000, v46
	v_min_f32_e32 v47, 0x40e00000, v47
	v_min_f32_e32 v48, 0x40e00000, v48
	v_min_f32_e32 v49, 0x40e00000, v49
	v_mul_f32_e32 v180, 0xc01d265f, v46
	v_mul_f32_e32 v181, 0xc01d265f, v47
	v_mul_f32_e32 v182, 0xc01d265f, v48
	v_mul_f32_e32 v183, 0xc01d265f, v49
	v_exp_f32_e32 v180, v180
	v_exp_f32_e32 v181, v181
	v_exp_f32_e32 v182, v182
	v_exp_f32_e32 v183, v183
	v_fmamk_f32 v42, v42, 0x3d000000, v91
	v_fmamk_f32 v43, v43, 0x3d000000, v93
	v_fmamk_f32 v44, v44, 0x3d000000, v83
	v_fmamk_f32 v45, v45, 0x3d000000, v85
	v_add_f32_e32 v180, 1.0, v180
	v_add_f32_e32 v181, 1.0, v181
	v_add_f32_e32 v182, 1.0, v182
	v_add_f32_e32 v183, 1.0, v183
	v_rcp_f32_e32 v180, v180
	v_rcp_f32_e32 v181, v181
	v_rcp_f32_e32 v182, v182
	v_rcp_f32_e32 v183, v183
	v_med3_f32 v42, v42, s72, v178
	v_med3_f32 v43, v43, s72, v178
	v_med3_f32 v44, v44, s72, v178
	v_med3_f32 v45, v45, s72, v178
	v_mul_f32_e32 v180, v46, v180
	v_mul_f32_e32 v181, v47, v181
	v_mul_f32_e32 v182, v48, v182
	v_mul_f32_e32 v183, v49, v183
	v_mul_f32_e32 v180, v42, v180
	v_mul_f32_e32 v181, v43, v181
	v_mul_f32_e32 v182, v44, v182
	v_mul_f32_e32 v183, v45, v183
	v_cvt_pk_fp8_f32 v190, v180, v181
	v_cvt_pk_fp8_f32 v190, v182, v183 op_sel:[0,0,1]
	v_fmamk_f32 v38, v38, 0x3d000000, v74
	v_fmamk_f32 v39, v39, 0x3d000000, v76
	v_fmamk_f32 v40, v40, 0x3d000000, v66
	v_fmamk_f32 v41, v41, 0x3d000000, v68
	v_min_f32_e32 v38, 0x40e00000, v38
	v_min_f32_e32 v39, 0x40e00000, v39
	v_min_f32_e32 v40, 0x40e00000, v40
	v_min_f32_e32 v41, 0x40e00000, v41
	v_mul_f32_e32 v184, 0xc01d265f, v38
	v_mul_f32_e32 v185, 0xc01d265f, v39
	v_mul_f32_e32 v186, 0xc01d265f, v40
	v_mul_f32_e32 v187, 0xc01d265f, v41
	v_exp_f32_e32 v184, v184
	v_exp_f32_e32 v185, v185
	v_exp_f32_e32 v186, v186
	v_exp_f32_e32 v187, v187
	v_fmamk_f32 v34, v34, 0x3d000000, v75
	v_fmamk_f32 v35, v35, 0x3d000000, v77
	v_fmamk_f32 v36, v36, 0x3d000000, v67
	v_fmamk_f32 v37, v37, 0x3d000000, v69
	v_add_f32_e32 v184, 1.0, v184
	v_add_f32_e32 v185, 1.0, v185
	v_add_f32_e32 v186, 1.0, v186
	v_add_f32_e32 v187, 1.0, v187
	v_rcp_f32_e32 v184, v184
	v_rcp_f32_e32 v185, v185
	v_rcp_f32_e32 v186, v186
	v_rcp_f32_e32 v187, v187
	v_med3_f32 v34, v34, s72, v178
	v_med3_f32 v35, v35, s72, v178
	v_med3_f32 v36, v36, s72, v178
	v_med3_f32 v37, v37, s72, v178
	v_mul_f32_e32 v184, v38, v184
	v_mul_f32_e32 v185, v39, v185
	v_mul_f32_e32 v186, v40, v186
	v_mul_f32_e32 v187, v41, v187
	v_mul_f32_e32 v184, v34, v184
	v_mul_f32_e32 v185, v35, v185
	v_mul_f32_e32 v186, v36, v186
	v_mul_f32_e32 v187, v37, v187
	v_cvt_pk_fp8_f32 v191, v184, v185
	v_cvt_pk_fp8_f32 v191, v186, v187 op_sel:[0,0,1]
	global_store_dwordx2 v[194:195], v[190:191], off
	s_mov_b32 s98, 0x28000
	v_lshl_add_u64 v[196:197], v[176:177], 0, s[98:99]
	v_fmamk_f32 v30, v30, 0x3d000000, v90
	v_fmamk_f32 v31, v31, 0x3d000000, v92
	v_fmamk_f32 v32, v32, 0x3d000000, v82
	v_fmamk_f32 v33, v33, 0x3d000000, v84
	v_min_f32_e32 v30, 0x40e00000, v30
	v_min_f32_e32 v31, 0x40e00000, v31
	v_min_f32_e32 v32, 0x40e00000, v32
	v_min_f32_e32 v33, 0x40e00000, v33
	v_mul_f32_e32 v180, 0xc01d265f, v30
	v_mul_f32_e32 v181, 0xc01d265f, v31
	v_mul_f32_e32 v182, 0xc01d265f, v32
	v_mul_f32_e32 v183, 0xc01d265f, v33
	v_exp_f32_e32 v180, v180
	v_exp_f32_e32 v181, v181
	v_exp_f32_e32 v182, v182
	v_exp_f32_e32 v183, v183
	v_fmamk_f32 v26, v26, 0x3d000000, v91
	v_fmamk_f32 v27, v27, 0x3d000000, v93
	v_fmamk_f32 v28, v28, 0x3d000000, v83
	v_fmamk_f32 v29, v29, 0x3d000000, v85
	v_add_f32_e32 v180, 1.0, v180
	v_add_f32_e32 v181, 1.0, v181
	v_add_f32_e32 v182, 1.0, v182
	v_add_f32_e32 v183, 1.0, v183
	v_rcp_f32_e32 v180, v180
	v_rcp_f32_e32 v181, v181
	v_rcp_f32_e32 v182, v182
	v_rcp_f32_e32 v183, v183
	v_med3_f32 v26, v26, s72, v178
	v_med3_f32 v27, v27, s72, v178
	v_med3_f32 v28, v28, s72, v178
	v_med3_f32 v29, v29, s72, v178
	v_mul_f32_e32 v180, v30, v180
	v_mul_f32_e32 v181, v31, v181
	v_mul_f32_e32 v182, v32, v182
	v_mul_f32_e32 v183, v33, v183
	v_mul_f32_e32 v180, v26, v180
	v_mul_f32_e32 v181, v27, v181
	v_mul_f32_e32 v182, v28, v182
	v_mul_f32_e32 v183, v29, v183
	v_cvt_pk_fp8_f32 v188, v180, v181
	v_cvt_pk_fp8_f32 v188, v182, v183 op_sel:[0,0,1]
	v_fmamk_f32 v22, v22, 0x3d000000, v74
	v_fmamk_f32 v23, v23, 0x3d000000, v76
	v_fmamk_f32 v24, v24, 0x3d000000, v66
	v_fmamk_f32 v25, v25, 0x3d000000, v68
	v_min_f32_e32 v22, 0x40e00000, v22
	v_min_f32_e32 v23, 0x40e00000, v23
	v_min_f32_e32 v24, 0x40e00000, v24
	v_min_f32_e32 v25, 0x40e00000, v25
	v_mul_f32_e32 v184, 0xc01d265f, v22
	v_mul_f32_e32 v185, 0xc01d265f, v23
	v_mul_f32_e32 v186, 0xc01d265f, v24
	v_mul_f32_e32 v187, 0xc01d265f, v25
	v_exp_f32_e32 v184, v184
	v_exp_f32_e32 v185, v185
	v_exp_f32_e32 v186, v186
	v_exp_f32_e32 v187, v187
	v_fmamk_f32 v18, v18, 0x3d000000, v75
	v_fmamk_f32 v19, v19, 0x3d000000, v77
	v_fmamk_f32 v20, v20, 0x3d000000, v67
	v_fmamk_f32 v21, v21, 0x3d000000, v69
	v_add_f32_e32 v184, 1.0, v184
	v_add_f32_e32 v185, 1.0, v185
	v_add_f32_e32 v186, 1.0, v186
	v_add_f32_e32 v187, 1.0, v187
	v_rcp_f32_e32 v184, v184
	v_rcp_f32_e32 v185, v185
	v_rcp_f32_e32 v186, v186
	v_rcp_f32_e32 v187, v187
	v_med3_f32 v18, v18, s72, v178
	v_med3_f32 v19, v19, s72, v178
	v_med3_f32 v20, v20, s72, v178
	v_med3_f32 v21, v21, s72, v178
	v_mul_f32_e32 v184, v22, v184
	v_mul_f32_e32 v185, v23, v185
	v_mul_f32_e32 v186, v24, v186
	v_mul_f32_e32 v187, v25, v187
	v_mul_f32_e32 v184, v18, v184
	v_mul_f32_e32 v185, v19, v185
	v_mul_f32_e32 v186, v20, v186
	v_mul_f32_e32 v187, v21, v187
	v_cvt_pk_fp8_f32 v189, v184, v185
	v_cvt_pk_fp8_f32 v189, v186, v187 op_sel:[0,0,1]
	global_store_dwordx2 v[196:197], v[188:189], off
	s_mov_b32 s98, 0x2c000
	v_lshl_add_u64 v[198:199], v[176:177], 0, s[98:99]
	v_fmamk_f32 v14, v14, 0x3d000000, v90
	v_fmamk_f32 v15, v15, 0x3d000000, v92
	v_fmamk_f32 v16, v16, 0x3d000000, v82
	v_fmamk_f32 v17, v17, 0x3d000000, v84
	v_min_f32_e32 v14, 0x40e00000, v14
	v_min_f32_e32 v15, 0x40e00000, v15
	v_min_f32_e32 v16, 0x40e00000, v16
	v_min_f32_e32 v17, 0x40e00000, v17
	v_mul_f32_e32 v180, 0xc01d265f, v14
	v_mul_f32_e32 v181, 0xc01d265f, v15
	v_mul_f32_e32 v182, 0xc01d265f, v16
	v_mul_f32_e32 v183, 0xc01d265f, v17
	v_exp_f32_e32 v180, v180
	v_exp_f32_e32 v181, v181
	v_exp_f32_e32 v182, v182
	v_exp_f32_e32 v183, v183
	v_fmamk_f32 v10, v10, 0x3d000000, v91
	v_fmamk_f32 v11, v11, 0x3d000000, v93
	v_fmamk_f32 v12, v12, 0x3d000000, v83
	v_fmamk_f32 v13, v13, 0x3d000000, v85
	v_add_f32_e32 v180, 1.0, v180
	v_add_f32_e32 v181, 1.0, v181
	v_add_f32_e32 v182, 1.0, v182
	v_add_f32_e32 v183, 1.0, v183
	v_rcp_f32_e32 v180, v180
	v_rcp_f32_e32 v181, v181
	v_rcp_f32_e32 v182, v182
	v_rcp_f32_e32 v183, v183
	v_med3_f32 v10, v10, s72, v178
	v_med3_f32 v11, v11, s72, v178
	v_med3_f32 v12, v12, s72, v178
	v_med3_f32 v13, v13, s72, v178
	v_mul_f32_e32 v180, v14, v180
	v_mul_f32_e32 v181, v15, v181
	v_mul_f32_e32 v182, v16, v182
	v_mul_f32_e32 v183, v17, v183
	v_mul_f32_e32 v180, v10, v180
	v_mul_f32_e32 v181, v11, v181
	v_mul_f32_e32 v182, v12, v182
	v_mul_f32_e32 v183, v13, v183
	v_cvt_pk_fp8_f32 v190, v180, v181
	v_cvt_pk_fp8_f32 v190, v182, v183 op_sel:[0,0,1]
	v_fmamk_f32 v6, v6, 0x3d000000, v74
	v_fmamk_f32 v7, v7, 0x3d000000, v76
	v_fmamk_f32 v8, v8, 0x3d000000, v66
	v_fmamk_f32 v9, v9, 0x3d000000, v68
	v_min_f32_e32 v6, 0x40e00000, v6
	v_min_f32_e32 v7, 0x40e00000, v7
	v_min_f32_e32 v8, 0x40e00000, v8
	v_min_f32_e32 v9, 0x40e00000, v9
	v_mul_f32_e32 v184, 0xc01d265f, v6
	v_mul_f32_e32 v185, 0xc01d265f, v7
	v_mul_f32_e32 v186, 0xc01d265f, v8
	v_mul_f32_e32 v187, 0xc01d265f, v9
	v_exp_f32_e32 v184, v184
	v_exp_f32_e32 v185, v185
	v_exp_f32_e32 v186, v186
	v_exp_f32_e32 v187, v187
	v_fmamk_f32 v2, v2, 0x3d000000, v75
	v_fmamk_f32 v3, v3, 0x3d000000, v77
	v_fmamk_f32 v4, v4, 0x3d000000, v67
	v_fmamk_f32 v5, v5, 0x3d000000, v69
	v_add_f32_e32 v184, 1.0, v184
	v_add_f32_e32 v185, 1.0, v185
	v_add_f32_e32 v186, 1.0, v186
	v_add_f32_e32 v187, 1.0, v187
	v_rcp_f32_e32 v184, v184
	v_rcp_f32_e32 v185, v185
	v_rcp_f32_e32 v186, v186
	v_rcp_f32_e32 v187, v187
	v_med3_f32 v2, v2, s72, v178
	v_med3_f32 v3, v3, s72, v178
	v_med3_f32 v4, v4, s72, v178
	v_med3_f32 v5, v5, s72, v178
	v_mul_f32_e32 v184, v6, v184
	v_mul_f32_e32 v185, v7, v185
	v_mul_f32_e32 v186, v8, v186
	v_mul_f32_e32 v187, v9, v187
	v_mul_f32_e32 v184, v2, v184
	v_mul_f32_e32 v185, v3, v185
	v_mul_f32_e32 v186, v4, v186
	v_mul_f32_e32 v187, v5, v187
	v_cvt_pk_fp8_f32 v191, v184, v185
	v_cvt_pk_fp8_f32 v191, v186, v187 op_sel:[0,0,1]
	global_store_dwordx2 v[198:199], v[190:191], off
	s_cbranch_vccnz .LBB0_1239
	s_andn2_b64 vcc, exec, s[10:11]
	s_cbranch_vccnz .LBB0_1238
	s_barrier
	s_branch .LBB0_1238
